# dpp5: dpp4 + the remaining combine-phase wave_sum chains via DPP
# baseline (speedup 1.0000x reference)
; __device__ __forceinline__ float bf_lo(unsigned w) { return __uint_as_float(w << 16); }
; __device__ __forceinline__ float bf_hi(unsigned w) { return __uint_as_float(w & 0xffff0000u); }
; __device__ __forceinline__ float wave_sum(float v) { return half_sum(sum32(v)); }
; __device__ __forceinline__ void st_bf4(bf16_t* p, f32x4 v) { u32x2 w; w.x = cvt_pk_bf16(v[0], v[1]); w.y = cvt_pk_bf16(v[2], v[3]); *(u32x2*)p = w; }
; template <int NTK>
; __device__ __forceinline__ void combine_rows(int t0, int tstride, const LAS int* bst, const int* tok_e, const int* tok_pos, const float* tok_w, const bf16_t* Y, const bf16_t* xbi, float* xio, bf16_t* xb, float* part, const float* gfin, bool last, int lane) {
;     ...
;     for (int i = 0; i < NTK; ++i) { float s = 0.f;
; #pragma unroll
;         for (int j = 0; j < 4; ++j) { const f32x4 a = {bf_lo(ya[i][j].x), bf_hi(ya[i][j].x), bf_lo(ya[i][j].y), bf_hi(ya[i][j].y)}, b = {bf_lo(yb[i][j].x), bf_hi(yb[i][j].x), bf_lo(yb[i][j].y), bf_hi(yb[i][j].y)};
;             v[i][j] = v[i][j] + w0[i] * a + w1[i] * b;
;             s += (v[i][j][0] * v[i][j][0] + v[i][j][1] * v[i][j][1]) + (v[i][j][2] * v[i][j][2] + v[i][j][3] * v[i][j][3]); }
;         s = wave_sum(s);
;         if (ok[i]) { const int t = tk[i];
;             if (!last) {
; #pragma unroll
;                 for (int j = 0; j < 4; ++j) { const int c = j * 256 + lane * 4; st_bf4(xb + (size_t)t * DM + c, v[i][j]); }
;                 if (lane < 16) part[(size_t)t * 16 + lane] = lane == 0 ? s : 0.f;
.LBB0_1639:
	s_waitcnt vmcnt(35)
	s_nop 0
	v_lshlrev_b32_e32 v82, 16, v94
	v_and_b32_e32 v83, 0xffff0000, v94
	v_lshlrev_b32_e32 v84, 16, v95
	v_and_b32_e32 v85, 0xffff0000, v95
	s_waitcnt vmcnt(34)
	v_lshlrev_b32_e32 v106, 16, v92
	v_and_b32_e32 v107, 0xffff0000, v92
	v_lshlrev_b32_e32 v92, 16, v93
	v_and_b32_e32 v93, 0xffff0000, v93
	s_waitcnt vmcnt(33)
	v_lshlrev_b32_e32 v108, 16, v90
	v_and_b32_e32 v109, 0xffff0000, v90
	v_lshlrev_b32_e32 v90, 16, v91
	v_and_b32_e32 v91, 0xffff0000, v91
	v_pk_fma_f32 v[82:83], v[64:65], v[106:107], v[82:83] op_sel_hi:[0,1,1]
	v_pk_fma_f32 v[84:85], v[64:65], v[92:93], v[84:85] op_sel_hi:[0,1,1]
	v_pk_fma_f32 v[90:91], v[64:65], v[90:91], v[84:85] op_sel:[1,0,0]
	v_pk_fma_f32 v[92:93], v[64:65], v[108:109], v[82:83] op_sel:[1,0,0]
	v_mul_f32_e32 v83, v91, v91
	v_mul_f32_e32 v82, v93, v93
	v_fmac_f32_e32 v82, v92, v92
	v_fmac_f32_e32 v83, v90, v90
	s_waitcnt vmcnt(32)
	v_lshlrev_b32_e32 v94, 16, v100
	v_and_b32_e32 v95, 0xffff0000, v100
	v_lshlrev_b32_e32 v100, 16, v101
	v_and_b32_e32 v101, 0xffff0000, v101
	v_add_f32_e32 v106, v82, v83
	s_waitcnt vmcnt(31)
	v_lshlrev_b32_e32 v82, 16, v88
	v_and_b32_e32 v83, 0xffff0000, v88
	v_lshlrev_b32_e32 v84, 16, v89
	v_and_b32_e32 v85, 0xffff0000, v89
	s_waitcnt vmcnt(30)
	v_lshlrev_b32_e32 v88, 16, v86
	v_and_b32_e32 v89, 0xffff0000, v86
	v_lshlrev_b32_e32 v86, 16, v87
	v_and_b32_e32 v87, 0xffff0000, v87
	v_pk_fma_f32 v[94:95], v[64:65], v[82:83], v[94:95] op_sel_hi:[0,1,1]
	v_pk_fma_f32 v[82:83], v[64:65], v[84:85], v[100:101] op_sel_hi:[0,1,1]
	v_pk_fma_f32 v[82:83], v[64:65], v[86:87], v[82:83] op_sel:[1,0,0]
	v_pk_fma_f32 v[84:85], v[64:65], v[88:89], v[94:95] op_sel:[1,0,0]
	v_mul_f32_e32 v87, v83, v83
	v_mul_f32_e32 v86, v85, v85
	v_fmac_f32_e32 v86, v84, v84
	v_fmac_f32_e32 v87, v82, v82
	v_add_f32_e32 v86, v86, v87
	s_waitcnt vmcnt(29)
	v_lshlrev_b32_e32 v102, 16, v98
	v_and_b32_e32 v103, 0xffff0000, v98
	v_lshlrev_b32_e32 v98, 16, v99
	v_and_b32_e32 v99, 0xffff0000, v99
	v_add_f32_e32 v94, v106, v86
	s_waitcnt vmcnt(28)
	v_lshlrev_b32_e32 v86, 16, v80
	v_and_b32_e32 v87, 0xffff0000, v80
	v_lshlrev_b32_e32 v80, 16, v81
	v_and_b32_e32 v81, 0xffff0000, v81
	s_waitcnt vmcnt(27)
	v_lshlrev_b32_e32 v88, 16, v78
	v_and_b32_e32 v89, 0xffff0000, v78
	v_lshlrev_b32_e32 v78, 16, v79
	v_and_b32_e32 v79, 0xffff0000, v79
	v_pk_fma_f32 v[86:87], v[64:65], v[86:87], v[102:103] op_sel_hi:[0,1,1]
	v_pk_fma_f32 v[80:81], v[64:65], v[80:81], v[98:99] op_sel_hi:[0,1,1]
	v_pk_fma_f32 v[78:79], v[64:65], v[78:79], v[80:81] op_sel:[1,0,0]
	v_pk_fma_f32 v[80:81], v[64:65], v[88:89], v[86:87] op_sel:[1,0,0]
	v_mul_f32_e32 v87, v79, v79
	v_mul_f32_e32 v86, v81, v81
	v_fmac_f32_e32 v86, v80, v80
	v_fmac_f32_e32 v87, v78, v78
	v_add_f32_e32 v86, v86, v87
	s_waitcnt vmcnt(26)
	v_lshlrev_b32_e32 v104, 16, v96
	v_and_b32_e32 v105, 0xffff0000, v96
	v_lshlrev_b32_e32 v96, 16, v97
	v_and_b32_e32 v97, 0xffff0000, v97
	v_add_f32_e32 v94, v94, v86
	s_waitcnt vmcnt(25)
	v_lshlrev_b32_e32 v86, 16, v76
	v_and_b32_e32 v87, 0xffff0000, v76
	v_lshlrev_b32_e32 v76, 16, v77
	v_and_b32_e32 v77, 0xffff0000, v77
	s_waitcnt vmcnt(24)
	v_lshlrev_b32_e32 v88, 16, v74
	v_and_b32_e32 v89, 0xffff0000, v74
	v_lshlrev_b32_e32 v74, 16, v75
	v_and_b32_e32 v75, 0xffff0000, v75
	v_pk_fma_f32 v[86:87], v[64:65], v[86:87], v[104:105] op_sel_hi:[0,1,1]
	v_pk_fma_f32 v[76:77], v[64:65], v[76:77], v[96:97] op_sel_hi:[0,1,1]
	v_pk_fma_f32 v[74:75], v[64:65], v[74:75], v[76:77] op_sel:[1,0,0]
	v_pk_fma_f32 v[64:65], v[64:65], v[88:89], v[86:87] op_sel:[1,0,0]
	v_mul_f32_e32 v77, v75, v75
	v_mul_f32_e32 v76, v65, v65
	v_fmac_f32_e32 v76, v64, v64
	v_fmac_f32_e32 v77, v74, v74
	v_add_f32_e32 v76, v76, v77
	v_add_f32_e32 v76, v94, v76
	s_andn2_b64 vcc, exec, s[28:29]
	s_waitcnt lgkmcnt(0)
	s_nop 1
	v_add_f32_dpp v76, v76, v76 quad_perm:[1,0,3,2] row_mask:0xf bank_mask:0xf
	s_waitcnt lgkmcnt(0)
	s_nop 1
	v_add_f32_dpp v76, v76, v76 quad_perm:[2,3,0,1] row_mask:0xf bank_mask:0xf
	s_waitcnt lgkmcnt(0)
	s_nop 1
	v_add_f32_dpp v76, v76, v76 row_half_mirror row_mask:0xf bank_mask:0xf
	s_waitcnt lgkmcnt(0)
	s_nop 1
	v_add_f32_dpp v76, v76, v76 row_mirror row_mask:0xf bank_mask:0xf
	v_mov_b32_e32 v77, v76
	s_waitcnt lgkmcnt(0)
	s_nop 1
	v_permlane16_swap_b32_e32 v77, v76
	v_add_f32_e32 v76, v76, v77
	v_mov_b32_e32 v77, v76
	s_nop 1
	v_permlane32_swap_b32_e32 v76, v77
	s_cbranch_vccnz .LBB0_1646
	v_add_f32_e32 v76, v76, v77
	s_and_b64 vcc, exec, s[6:7]
	s_mov_b64 s[10:11], -1
	s_cbranch_vccnz .LBB0_1644
	v_cvt_pk_bf16_f32 v86, v92, v93
	v_cvt_pk_bf16_f32 v87, v90, v91
	global_store_dwordx2 v[72:73], v[86:87], off
	v_cvt_pk_bf16_f32 v86, v84, v85
	v_cvt_pk_bf16_f32 v87, v82, v83
	global_store_dwordx2 v[72:73], v[86:87], off offset:512
	v_cvt_pk_bf16_f32 v86, v80, v81
	v_cvt_pk_bf16_f32 v87, v78, v79
	global_store_dwordx2 v[72:73], v[86:87], off offset:1024
	v_cvt_pk_bf16_f32 v86, v64, v65
	v_cvt_pk_bf16_f32 v87, v74, v75
	global_store_dwordx2 v[72:73], v[86:87], off offset:1536
	s_and_saveexec_b64 s[10:11], s[0:1]
	s_cbranch_execz .LBB0_1643
	s_lshl_b64 s[2:3], s[26:27], 6
	v_cndmask_b32_e64 v77, 0, v76, s[4:5]
	v_lshl_add_u64 v[72:73], v[0:1], 0, s[2:3]
	global_store_dword v[72:73], v77, off

; __device__ __forceinline__ float bf_lo(unsigned w) { return __uint_as_float(w << 16); }
; __device__ __forceinline__ float bf_hi(unsigned w) { return __uint_as_float(w & 0xffff0000u); }
; __device__ __forceinline__ float wave_sum(float v) { return half_sum(sum32(v)); }
; __device__ __forceinline__ void st_bf4(bf16_t* p, f32x4 v) { u32x2 w; w.x = cvt_pk_bf16(v[0], v[1]); w.y = cvt_pk_bf16(v[2], v[3]); *(u32x2*)p = w; }
; template <int NTK>
; __device__ __forceinline__ void combine_rows(int t0, int tstride, const LAS int* bst, const int* tok_e, const int* tok_pos, const float* tok_w, const bf16_t* Y, const bf16_t* xbi, float* xio, bf16_t* xb, float* part, const float* gfin, bool last, int lane) {
;     ...
;     for (int i = 0; i < NTK; ++i) { float s = 0.f;
; #pragma unroll
;         for (int j = 0; j < 4; ++j) { const f32x4 a = {bf_lo(ya[i][j].x), bf_hi(ya[i][j].x), bf_lo(ya[i][j].y), bf_hi(ya[i][j].y)}, b = {bf_lo(yb[i][j].x), bf_hi(yb[i][j].x), bf_lo(yb[i][j].y), bf_hi(yb[i][j].y)};
;             v[i][j] = v[i][j] + w0[i] * a + w1[i] * b;
;             s += (v[i][j][0] * v[i][j][0] + v[i][j][1] * v[i][j][1]) + (v[i][j][2] * v[i][j][2] + v[i][j][3] * v[i][j][3]); }
;         s = wave_sum(s);
;         if (ok[i]) { const int t = tk[i];
;             if (!last) {
; #pragma unroll
;                 for (int j = 0; j < 4; ++j) { const int c = j * 256 + lane * 4; st_bf4(xb + (size_t)t * DM + c, v[i][j]); }
;                 if (lane < 16) part[(size_t)t * 16 + lane] = lane == 0 ? s : 0.f;
.LBB0_1646:
	s_waitcnt vmcnt(23)
	v_lshlrev_b32_e32 v64, 16, v56
	v_and_b32_e32 v65, 0xffff0000, v56
	v_lshlrev_b32_e32 v56, 16, v57
	v_and_b32_e32 v57, 0xffff0000, v57
	s_waitcnt vmcnt(22)
	v_lshlrev_b32_e32 v78, 16, v54
	v_and_b32_e32 v79, 0xffff0000, v54
	v_lshlrev_b32_e32 v54, 16, v55
	v_and_b32_e32 v55, 0xffff0000, v55
	s_waitcnt vmcnt(21)
	v_lshlrev_b32_e32 v80, 16, v52
	v_and_b32_e32 v81, 0xffff0000, v52
	v_lshlrev_b32_e32 v52, 16, v53
	v_and_b32_e32 v53, 0xffff0000, v53
	v_pk_fma_f32 v[64:65], v[16:17], v[78:79], v[64:65] op_sel_hi:[0,1,1]
	v_pk_fma_f32 v[54:55], v[16:17], v[54:55], v[56:57] op_sel_hi:[0,1,1]
	v_pk_fma_f32 v[52:53], v[16:17], v[52:53], v[54:55] op_sel:[1,0,0]
	v_pk_fma_f32 v[54:55], v[16:17], v[80:81], v[64:65] op_sel:[1,0,0]
	v_mul_f32_e32 v57, v53, v53
	v_mul_f32_e32 v56, v55, v55
	v_fmac_f32_e32 v56, v54, v54
	v_fmac_f32_e32 v57, v52, v52
	s_waitcnt vmcnt(20)
	v_lshlrev_b32_e32 v72, 16, v62
	v_and_b32_e32 v73, 0xffff0000, v62
	v_lshlrev_b32_e32 v62, 16, v63
	v_and_b32_e32 v63, 0xffff0000, v63
	v_add_f32_e32 v78, v56, v57
	s_waitcnt vmcnt(19)
	v_lshlrev_b32_e32 v56, 16, v50
	v_and_b32_e32 v57, 0xffff0000, v50
	v_lshlrev_b32_e32 v50, 16, v51
	v_and_b32_e32 v51, 0xffff0000, v51
	s_waitcnt vmcnt(18)
	v_lshlrev_b32_e32 v64, 16, v48
	v_and_b32_e32 v65, 0xffff0000, v48
	v_lshlrev_b32_e32 v48, 16, v49
	v_and_b32_e32 v49, 0xffff0000, v49
	v_pk_fma_f32 v[56:57], v[16:17], v[56:57], v[72:73] op_sel_hi:[0,1,1]
	v_pk_fma_f32 v[50:51], v[16:17], v[50:51], v[62:63] op_sel_hi:[0,1,1]
	v_pk_fma_f32 v[48:49], v[16:17], v[48:49], v[50:51] op_sel:[1,0,0]
	v_pk_fma_f32 v[50:51], v[16:17], v[64:65], v[56:57] op_sel:[1,0,0]
	v_mul_f32_e32 v57, v49, v49
	v_mul_f32_e32 v56, v51, v51
	v_fmac_f32_e32 v56, v50, v50
	v_fmac_f32_e32 v57, v48, v48
	v_add_f32_e32 v56, v56, v57
	s_waitcnt vmcnt(17)
	v_lshlrev_b32_e32 v74, 16, v60
	v_and_b32_e32 v75, 0xffff0000, v60
	v_lshlrev_b32_e32 v60, 16, v61
	v_and_b32_e32 v61, 0xffff0000, v61
	v_add_f32_e32 v64, v78, v56
	s_waitcnt vmcnt(16)
	v_lshlrev_b32_e32 v56, 16, v46
	v_and_b32_e32 v57, 0xffff0000, v46
	v_lshlrev_b32_e32 v46, 16, v47
	v_and_b32_e32 v47, 0xffff0000, v47
	s_waitcnt vmcnt(15)
	v_lshlrev_b32_e32 v62, 16, v44
	v_and_b32_e32 v63, 0xffff0000, v44
	v_lshlrev_b32_e32 v44, 16, v45
	v_and_b32_e32 v45, 0xffff0000, v45
	v_pk_fma_f32 v[56:57], v[16:17], v[56:57], v[74:75] op_sel_hi:[0,1,1]
	v_pk_fma_f32 v[46:47], v[16:17], v[46:47], v[60:61] op_sel_hi:[0,1,1]
	v_pk_fma_f32 v[44:45], v[16:17], v[44:45], v[46:47] op_sel:[1,0,0]
	v_pk_fma_f32 v[46:47], v[16:17], v[62:63], v[56:57] op_sel:[1,0,0]
	v_mul_f32_e32 v57, v45, v45
	v_mul_f32_e32 v56, v47, v47
	v_fmac_f32_e32 v56, v46, v46
	v_fmac_f32_e32 v57, v44, v44
	v_add_f32_e32 v56, v56, v57
	s_waitcnt vmcnt(14)
	v_lshlrev_b32_e32 v76, 16, v58
	v_and_b32_e32 v77, 0xffff0000, v58
	v_lshlrev_b32_e32 v58, 16, v59
	v_and_b32_e32 v59, 0xffff0000, v59
	v_add_f32_e32 v62, v64, v56
	s_waitcnt vmcnt(13)
	v_lshlrev_b32_e32 v56, 16, v38
	v_and_b32_e32 v57, 0xffff0000, v38
	v_lshlrev_b32_e32 v38, 16, v39
	v_and_b32_e32 v39, 0xffff0000, v39
	s_waitcnt vmcnt(12)
	v_lshlrev_b32_e32 v60, 16, v36
	v_and_b32_e32 v61, 0xffff0000, v36
	v_lshlrev_b32_e32 v36, 16, v37
	v_and_b32_e32 v37, 0xffff0000, v37
	v_pk_fma_f32 v[56:57], v[16:17], v[56:57], v[76:77] op_sel_hi:[0,1,1]
	v_pk_fma_f32 v[38:39], v[16:17], v[38:39], v[58:59] op_sel_hi:[0,1,1]
	v_pk_fma_f32 v[36:37], v[16:17], v[36:37], v[38:39] op_sel:[1,0,0]
	v_pk_fma_f32 v[16:17], v[16:17], v[60:61], v[56:57] op_sel:[1,0,0]
	v_mul_f32_e32 v39, v37, v37
	v_mul_f32_e32 v38, v17, v17
	v_fmac_f32_e32 v38, v16, v16
	v_fmac_f32_e32 v39, v36, v36
	v_add_f32_e32 v38, v38, v39
	v_add_f32_e32 v38, v62, v38
	s_andn2_b64 vcc, exec, s[24:25]
	s_waitcnt lgkmcnt(0)
	s_nop 1
	v_add_f32_dpp v38, v38, v38 quad_perm:[1,0,3,2] row_mask:0xf bank_mask:0xf
	s_waitcnt lgkmcnt(0)
	s_nop 1
	v_add_f32_dpp v38, v38, v38 quad_perm:[2,3,0,1] row_mask:0xf bank_mask:0xf
	s_waitcnt lgkmcnt(0)
	s_nop 1
	v_add_f32_dpp v38, v38, v38 row_half_mirror row_mask:0xf bank_mask:0xf
	s_waitcnt lgkmcnt(0)
	s_nop 1
	v_add_f32_dpp v38, v38, v38 row_mirror row_mask:0xf bank_mask:0xf
	v_mov_b32_e32 v39, v38
	s_waitcnt lgkmcnt(0)
	s_nop 1
	v_permlane16_swap_b32_e32 v39, v38
	v_add_f32_e32 v38, v38, v39
	v_mov_b32_e32 v39, v38
	s_nop 1
	v_permlane32_swap_b32_e32 v38, v39
	s_cbranch_vccnz .LBB0_1653
	v_add_f32_e32 v38, v38, v39
	s_and_b64 vcc, exec, s[6:7]
	s_mov_b64 s[10:11], -1
	s_cbranch_vccnz .LBB0_1651
	v_cvt_pk_bf16_f32 v56, v54, v55
	v_cvt_pk_bf16_f32 v57, v52, v53
	global_store_dwordx2 v[20:21], v[56:57], off
	v_cvt_pk_bf16_f32 v56, v50, v51
	v_cvt_pk_bf16_f32 v57, v48, v49
	global_store_dwordx2 v[20:21], v[56:57], off offset:512
	v_cvt_pk_bf16_f32 v56, v46, v47
	v_cvt_pk_bf16_f32 v57, v44, v45
	global_store_dwordx2 v[20:21], v[56:57], off offset:1024
	v_cvt_pk_bf16_f32 v56, v16, v17
	v_cvt_pk_bf16_f32 v57, v36, v37
	global_store_dwordx2 v[20:21], v[56:57], off offset:1536
	s_and_saveexec_b64 s[10:11], s[0:1]
	s_cbranch_execz .LBB0_1650
	s_lshl_b64 s[2:3], s[22:23], 6
	v_cndmask_b32_e64 v39, 0, v38, s[4:5]
	v_lshl_add_u64 v[20:21], v[0:1], 0, s[2:3]
	global_store_dword v[20:21], v39, off

; __device__ __forceinline__ float bf_lo(unsigned w) { return __uint_as_float(w << 16); }
; __device__ __forceinline__ float bf_hi(unsigned w) { return __uint_as_float(w & 0xffff0000u); }
; __device__ __forceinline__ float wave_sum(float v) { return half_sum(sum32(v)); }
; __device__ __forceinline__ void st_bf4(bf16_t* p, f32x4 v) { u32x2 w; w.x = cvt_pk_bf16(v[0], v[1]); w.y = cvt_pk_bf16(v[2], v[3]); *(u32x2*)p = w; }
; template <int NTK>
; __device__ __forceinline__ void combine_rows(int t0, int tstride, const LAS int* bst, const int* tok_e, const int* tok_pos, const float* tok_w, const bf16_t* Y, const bf16_t* xbi, float* xio, bf16_t* xb, float* part, const float* gfin, bool last, int lane) {
;     ...
;     for (int i = 0; i < NTK; ++i) { float s = 0.f;
; #pragma unroll
;         for (int j = 0; j < 4; ++j) { const f32x4 a = {bf_lo(ya[i][j].x), bf_hi(ya[i][j].x), bf_lo(ya[i][j].y), bf_hi(ya[i][j].y)}, b = {bf_lo(yb[i][j].x), bf_hi(yb[i][j].x), bf_lo(yb[i][j].y), bf_hi(yb[i][j].y)};
;             v[i][j] = v[i][j] + w0[i] * a + w1[i] * b;
;             s += (v[i][j][0] * v[i][j][0] + v[i][j][1] * v[i][j][1]) + (v[i][j][2] * v[i][j][2] + v[i][j][3] * v[i][j][3]); }
;         s = wave_sum(s);
;         if (ok[i]) { const int t = tk[i];
;             if (!last) {
; #pragma unroll
;                 for (int j = 0; j < 4; ++j) { const int c = j * 256 + lane * 4; st_bf4(xb + (size_t)t * DM + c, v[i][j]); }
;                 if (lane < 16) part[(size_t)t * 16 + lane] = lane == 0 ? s : 0.f;
.LBB0_1653:
	s_waitcnt vmcnt(11)
	v_lshlrev_b32_e32 v16, 16, v32
	v_and_b32_e32 v17, 0xffff0000, v32
	v_lshlrev_b32_e32 v20, 16, v33
	v_and_b32_e32 v21, 0xffff0000, v33
	s_waitcnt vmcnt(10)
	v_lshlrev_b32_e32 v32, 16, v30
	v_and_b32_e32 v33, 0xffff0000, v30
	v_lshlrev_b32_e32 v30, 16, v31
	v_and_b32_e32 v31, 0xffff0000, v31
	s_waitcnt vmcnt(9)
	v_lshlrev_b32_e32 v48, 16, v34
	v_and_b32_e32 v49, 0xffff0000, v34
	v_lshlrev_b32_e32 v34, 16, v35
	v_and_b32_e32 v35, 0xffff0000, v35
	v_pk_fma_f32 v[16:17], v[14:15], v[32:33], v[16:17] op_sel_hi:[0,1,1]
	v_pk_fma_f32 v[20:21], v[14:15], v[30:31], v[20:21] op_sel_hi:[0,1,1]
	v_pk_fma_f32 v[30:31], v[14:15], v[34:35], v[20:21] op_sel:[1,0,0]
	v_pk_fma_f32 v[32:33], v[14:15], v[48:49], v[16:17] op_sel:[1,0,0]
	v_mul_f32_e32 v17, v31, v31
	v_mul_f32_e32 v16, v33, v33
	v_fmac_f32_e32 v16, v32, v32
	v_fmac_f32_e32 v17, v30, v30
	s_waitcnt vmcnt(8)
	v_lshlrev_b32_e32 v36, 16, v40
	v_and_b32_e32 v37, 0xffff0000, v40
	v_lshlrev_b32_e32 v38, 16, v41
	v_and_b32_e32 v39, 0xffff0000, v41
	v_add_f32_e32 v48, v16, v17
	s_waitcnt vmcnt(7)
	v_lshlrev_b32_e32 v16, 16, v26
	v_and_b32_e32 v17, 0xffff0000, v26
	v_lshlrev_b32_e32 v20, 16, v27
	v_and_b32_e32 v21, 0xffff0000, v27
	s_waitcnt vmcnt(6)
	v_lshlrev_b32_e32 v26, 16, v28
	v_and_b32_e32 v27, 0xffff0000, v28
	v_lshlrev_b32_e32 v28, 16, v29
	v_and_b32_e32 v29, 0xffff0000, v29
	v_pk_fma_f32 v[34:35], v[14:15], v[16:17], v[36:37] op_sel_hi:[0,1,1]
	v_pk_fma_f32 v[16:17], v[14:15], v[20:21], v[38:39] op_sel_hi:[0,1,1]
	v_pk_fma_f32 v[16:17], v[14:15], v[28:29], v[16:17] op_sel:[1,0,0]
	v_pk_fma_f32 v[26:27], v[14:15], v[26:27], v[34:35] op_sel:[1,0,0]
	v_mul_f32_e32 v21, v17, v17
	v_mul_f32_e32 v20, v27, v27
	v_fmac_f32_e32 v20, v26, v26
	v_fmac_f32_e32 v21, v16, v16
	v_add_f32_e32 v20, v20, v21
	s_waitcnt vmcnt(5)
	v_lshlrev_b32_e32 v40, 16, v42
	v_and_b32_e32 v41, 0xffff0000, v42
	v_lshlrev_b32_e32 v42, 16, v43
	v_and_b32_e32 v43, 0xffff0000, v43
	v_add_f32_e32 v36, v48, v20
	s_waitcnt vmcnt(4)
	v_lshlrev_b32_e32 v20, 16, v22
	v_and_b32_e32 v21, 0xffff0000, v22
	v_lshlrev_b32_e32 v22, 16, v23
	v_and_b32_e32 v23, 0xffff0000, v23
	s_waitcnt vmcnt(3)
	v_lshlrev_b32_e32 v28, 16, v24
	v_and_b32_e32 v29, 0xffff0000, v24
	v_lshlrev_b32_e32 v24, 16, v25
	v_and_b32_e32 v25, 0xffff0000, v25
	v_pk_fma_f32 v[34:35], v[14:15], v[20:21], v[40:41] op_sel_hi:[0,1,1]
	v_pk_fma_f32 v[20:21], v[14:15], v[22:23], v[42:43] op_sel_hi:[0,1,1]
	v_pk_fma_f32 v[20:21], v[14:15], v[24:25], v[20:21] op_sel:[1,0,0]
	v_pk_fma_f32 v[24:25], v[14:15], v[28:29], v[34:35] op_sel:[1,0,0]
	v_mul_f32_e32 v23, v21, v21
	v_mul_f32_e32 v22, v25, v25
	v_fmac_f32_e32 v22, v24, v24
	v_fmac_f32_e32 v23, v20, v20
	v_add_f32_e32 v22, v22, v23
	s_waitcnt vmcnt(2)
	v_lshlrev_b32_e32 v44, 16, v70
	v_and_b32_e32 v45, 0xffff0000, v70
	v_lshlrev_b32_e32 v46, 16, v71
	v_and_b32_e32 v47, 0xffff0000, v71
	v_add_f32_e32 v40, v36, v22
	s_waitcnt vmcnt(1)
	v_lshlrev_b32_e32 v22, 16, v66
	v_and_b32_e32 v23, 0xffff0000, v66
	v_lshlrev_b32_e32 v28, 16, v67
	v_and_b32_e32 v29, 0xffff0000, v67
	s_waitcnt vmcnt(0)
	v_lshlrev_b32_e32 v34, 16, v68
	v_and_b32_e32 v35, 0xffff0000, v68
	v_lshlrev_b32_e32 v36, 16, v69
	v_and_b32_e32 v37, 0xffff0000, v69
	v_pk_fma_f32 v[38:39], v[14:15], v[22:23], v[44:45] op_sel_hi:[0,1,1]
	v_pk_fma_f32 v[22:23], v[14:15], v[28:29], v[46:47] op_sel_hi:[0,1,1]
	v_pk_fma_f32 v[22:23], v[14:15], v[36:37], v[22:23] op_sel:[1,0,0]
	v_pk_fma_f32 v[14:15], v[14:15], v[34:35], v[38:39] op_sel:[1,0,0]
	v_mul_f32_e32 v29, v23, v23
	v_mul_f32_e32 v28, v15, v15
	v_fmac_f32_e32 v28, v14, v14
	v_fmac_f32_e32 v29, v22, v22
	v_add_f32_e32 v28, v28, v29
	v_add_f32_e32 v28, v40, v28
	s_andn2_b64 vcc, exec, s[20:21]
	s_waitcnt lgkmcnt(0)
	s_nop 1
	v_add_f32_dpp v28, v28, v28 quad_perm:[1,0,3,2] row_mask:0xf bank_mask:0xf
	s_waitcnt lgkmcnt(0)
	s_nop 1
	v_add_f32_dpp v28, v28, v28 quad_perm:[2,3,0,1] row_mask:0xf bank_mask:0xf
	s_waitcnt lgkmcnt(0)
	s_nop 1
	v_add_f32_dpp v28, v28, v28 row_half_mirror row_mask:0xf bank_mask:0xf
	s_waitcnt lgkmcnt(0)
	s_nop 1
	v_add_f32_dpp v28, v28, v28 row_mirror row_mask:0xf bank_mask:0xf
	v_mov_b32_e32 v29, v28
	s_waitcnt lgkmcnt(0)
	s_nop 1
	v_permlane16_swap_b32_e32 v29, v28
	v_add_f32_e32 v28, v28, v29
	v_mov_b32_e32 v29, v28
	s_nop 1
	v_permlane32_swap_b32_e32 v28, v29
	s_cbranch_vccnz .LBB0_1632
	v_add_f32_e32 v28, v28, v29
	s_and_b64 vcc, exec, s[6:7]
	s_mov_b64 s[6:7], -1
	s_cbranch_vccnz .LBB0_1658
	v_cvt_pk_bf16_f32 v34, v32, v33
	v_cvt_pk_bf16_f32 v35, v30, v31
	global_store_dwordx2 v[18:19], v[34:35], off
	v_cvt_pk_bf16_f32 v34, v26, v27
	v_cvt_pk_bf16_f32 v35, v16, v17
	global_store_dwordx2 v[18:19], v[34:35], off offset:512
	v_cvt_pk_bf16_f32 v34, v24, v25
	v_cvt_pk_bf16_f32 v35, v20, v21
	global_store_dwordx2 v[18:19], v[34:35], off offset:1024
	v_cvt_pk_bf16_f32 v34, v14, v15
	v_cvt_pk_bf16_f32 v35, v22, v23
	global_store_dwordx2 v[18:19], v[34:35], off offset:1536
	s_and_saveexec_b64 s[6:7], s[0:1]
	s_cbranch_execz .LBB0_1657
	s_lshl_b64 s[2:3], s[18:19], 6
	v_cndmask_b32_e64 v29, 0, v28, s[4:5]
	v_lshl_add_u64 v[18:19], v[0:1], 0, s[2:3]
	global_store_dword v[18:19], v29, off
